# baseline (speedup 1.0000x reference)
.LBB1_3:
	s_add_i32 s20, s20, 1
	s_add_i32 s18, s18, 2
	s_cmp_eq_u32 s20, 30
	s_waitcnt lgkmcnt(0)
	s_barrier
	s_cbranch_scc1 .Lt30
